# P9 expert GEMM: next-unit rowtok gathers issued back to back without the four in-K-loop vmcnt(0) drains (offsets formed one K-iteration later); gate/up bias loads prefetched in the last K-iteration so
# speedup vs baseline: 1.4314x; 1.0143x over previous
.LBB0_1353:
	s_lshl_b64 s[6:7], s[26:27], 16
	s_lshl_b32 s27, s26, 2
	s_add_i32 s27, s27, 0
	s_add_i32 s27, s27, 0x21040
	s_add_u32 s42, s25, s6
	v_mov_b32_e32 v34, 0
	v_mov_b32_e32 v169, v163
	v_mov_b32_e32 v173, v163
	s_addc_u32 s43, s56, s7
	s_mov_b32 s29, -2
	s_mov_b64 s[44:45], s[2:3]
	v_mov_b32_e32 v35, v34
	v_mov_b32_e32 v36, v34
	v_mov_b32_e32 v37, v34
	v_mov_b32_e32 v42, v34
	v_mov_b32_e32 v43, v34
	v_mov_b32_e32 v44, v34
	v_mov_b32_e32 v45, v34
	v_mov_b32_e32 v50, v34
	v_mov_b32_e32 v51, v34
	v_mov_b32_e32 v52, v34
	v_mov_b32_e32 v53, v34
	v_mov_b32_e32 v58, v34
	v_mov_b32_e32 v59, v34
	v_mov_b32_e32 v60, v34
	v_mov_b32_e32 v61, v34
	v_mov_b32_e32 v66, v34
	v_mov_b32_e32 v67, v34
	v_mov_b32_e32 v68, v34
	v_mov_b32_e32 v69, v34
	v_mov_b32_e32 v74, v34
	v_mov_b32_e32 v75, v34
	v_mov_b32_e32 v76, v34
	v_mov_b32_e32 v77, v34
	v_mov_b32_e32 v82, v34
	v_mov_b32_e32 v83, v34
	v_mov_b32_e32 v84, v34
	v_mov_b32_e32 v85, v34
	v_mov_b32_e32 v90, v34
	v_mov_b32_e32 v91, v34
	v_mov_b32_e32 v92, v34
	v_mov_b32_e32 v93, v34
	v_mov_b32_e32 v38, v34
	v_mov_b32_e32 v39, v34
	v_mov_b32_e32 v40, v34
	v_mov_b32_e32 v41, v34
	v_mov_b32_e32 v46, v34
	v_mov_b32_e32 v47, v34
	v_mov_b32_e32 v48, v34
	v_mov_b32_e32 v49, v34
	v_mov_b32_e32 v54, v34
	v_mov_b32_e32 v55, v34
	v_mov_b32_e32 v56, v34
	v_mov_b32_e32 v57, v34
	v_mov_b32_e32 v62, v34
	v_mov_b32_e32 v63, v34
	v_mov_b32_e32 v64, v34
	v_mov_b32_e32 v65, v34
	v_mov_b32_e32 v70, v34
	v_mov_b32_e32 v71, v34
	v_mov_b32_e32 v72, v34
	v_mov_b32_e32 v73, v34
	v_mov_b32_e32 v78, v34
	v_mov_b32_e32 v79, v34
	v_mov_b32_e32 v80, v34
	v_mov_b32_e32 v81, v34
	v_mov_b32_e32 v86, v34
	v_mov_b32_e32 v87, v34
	v_mov_b32_e32 v88, v34
	v_mov_b32_e32 v89, v34
	v_mov_b32_e32 v94, v34
	v_mov_b32_e32 v95, v34
	v_mov_b32_e32 v96, v34
	v_mov_b32_e32 v97, v34
	v_mov_b32_e32 v98, v34
	v_mov_b32_e32 v99, v34
	v_mov_b32_e32 v100, v34
	v_mov_b32_e32 v101, v34
	v_mov_b32_e32 v106, v34
	v_mov_b32_e32 v107, v34
	v_mov_b32_e32 v108, v34
	v_mov_b32_e32 v109, v34
	v_mov_b32_e32 v114, v34
	v_mov_b32_e32 v115, v34
	v_mov_b32_e32 v116, v34
	v_mov_b32_e32 v117, v34
	v_mov_b32_e32 v122, v34
	v_mov_b32_e32 v123, v34
	v_mov_b32_e32 v124, v34
	v_mov_b32_e32 v125, v34
	v_mov_b32_e32 v130, v34
	v_mov_b32_e32 v131, v34
	v_mov_b32_e32 v132, v34
	v_mov_b32_e32 v133, v34
	v_mov_b32_e32 v138, v34
	v_mov_b32_e32 v139, v34
	v_mov_b32_e32 v140, v34
	v_mov_b32_e32 v141, v34
	v_mov_b32_e32 v146, v34
	v_mov_b32_e32 v147, v34
	v_mov_b32_e32 v148, v34
	v_mov_b32_e32 v149, v34
	v_mov_b32_e32 v150, v34
	v_mov_b32_e32 v151, v34
	v_mov_b32_e32 v152, v34
	v_mov_b32_e32 v153, v34
	v_mov_b32_e32 v102, v34
	v_mov_b32_e32 v103, v34
	v_mov_b32_e32 v104, v34
	v_mov_b32_e32 v105, v34
	v_mov_b32_e32 v110, v34
	v_mov_b32_e32 v111, v34
	v_mov_b32_e32 v112, v34
	v_mov_b32_e32 v113, v34
	v_mov_b32_e32 v118, v34
	v_mov_b32_e32 v119, v34
	v_mov_b32_e32 v120, v34
	v_mov_b32_e32 v121, v34
	v_mov_b32_e32 v126, v34
	v_mov_b32_e32 v127, v34
	v_mov_b32_e32 v128, v34
	v_mov_b32_e32 v129, v34
	v_mov_b32_e32 v134, v34
	v_mov_b32_e32 v135, v34
	v_mov_b32_e32 v136, v34
	v_mov_b32_e32 v137, v34
	v_mov_b32_e32 v142, v34
	v_mov_b32_e32 v143, v34
	v_mov_b32_e32 v144, v34
	v_mov_b32_e32 v145, v34
	v_mov_b32_e32 v154, v34
	v_mov_b32_e32 v155, v34
	v_mov_b32_e32 v156, v34
	v_mov_b32_e32 v157, v34
	v_mov_b32_e32 v158, v34
	v_mov_b32_e32 v159, v34
	v_mov_b32_e32 v160, v34
	v_mov_b32_e32 v161, v34
	s_branch .LBB0_1356
.LBB0_1355:
	v_add_u32_e32 v2, s85, v185
	v_add_u32_e32 v14, s86, v185
	ds_read_b128 v[18:21], v2
	ds_read_b128 v[22:25], v2 offset:1024
	ds_read_b128 v[26:29], v2 offset:2048
	ds_read_b128 v[30:33], v2 offset:3072
	ds_read_b128 v[2:5], v14
	ds_read_b128 v[6:9], v14 offset:1024
	ds_read_b128 v[10:13], v14 offset:2048
	ds_read_b128 v[14:17], v14 offset:3072
	v_lshl_add_u64 v[222:223], s[50:51], 0, v[168:169]
	s_add_i32 m0, s59, 0xc000
	ds_read_b128 v[174:177], v188
	ds_read_b128 v[178:181], v188 offset:1024
	ds_read_b128 v[198:201], v188 offset:2048
	ds_read_b128 v[202:205], v188 offset:3072
	ds_read_b128 v[206:209], v188 offset:4096
	ds_read_b128 v[210:213], v188 offset:5120
	ds_read_b128 v[214:217], v188 offset:6144
	ds_read_b128 v[218:221], v188 offset:7168
	global_load_lds_dwordx4 v[222:223], off
	v_lshl_add_u64 v[222:223], s[50:51], 0, v[172:173]
	s_add_i32 m0, s59, 0xe000
	s_nop 0
	global_load_lds_dwordx4 v[222:223], off
	s_waitcnt vmcnt(8)
	s_waitcnt lgkmcnt(0)
	s_barrier
	s_setprio 1
	s_waitcnt lgkmcnt(0)
	v_mfma_f32_16x16x128_f8f6f4 v[158:161], v[18:25], v[174:181], v[158:161]
	v_mfma_f32_16x16x128_f8f6f4 v[154:157], v[26:33], v[174:181], v[154:157]
	v_mfma_f32_16x16x128_f8f6f4 v[142:145], v[18:25], v[198:205], v[142:145]
	v_mfma_f32_16x16x128_f8f6f4 v[134:137], v[26:33], v[198:205], v[134:137]
	v_mfma_f32_16x16x128_f8f6f4 v[126:129], v[18:25], v[206:213], v[126:129]
	v_mfma_f32_16x16x128_f8f6f4 v[118:121], v[26:33], v[206:213], v[118:121]
	v_mfma_f32_16x16x128_f8f6f4 v[110:113], v[18:25], v[214:221], v[110:113]
	v_mfma_f32_16x16x128_f8f6f4 v[102:105], v[26:33], v[214:221], v[102:105]
	s_setprio 0
	s_setprio 1
	v_mfma_f32_16x16x128_f8f6f4 v[150:153], v[2:9], v[174:181], v[150:153]
	v_mfma_f32_16x16x128_f8f6f4 v[146:149], v[10:17], v[174:181], v[146:149]
	v_mfma_f32_16x16x128_f8f6f4 v[138:141], v[2:9], v[198:205], v[138:141]
	v_mfma_f32_16x16x128_f8f6f4 v[130:133], v[10:17], v[198:205], v[130:133]
	v_mfma_f32_16x16x128_f8f6f4 v[122:125], v[2:9], v[206:213], v[122:125]
	v_mfma_f32_16x16x128_f8f6f4 v[114:117], v[10:17], v[206:213], v[114:117]
	v_mfma_f32_16x16x128_f8f6f4 v[106:109], v[2:9], v[214:221], v[106:109]
	v_mfma_f32_16x16x128_f8f6f4 v[98:101], v[10:17], v[214:221], v[98:101]
	s_setprio 0
	s_barrier
	s_add_i32 s37, s85, s58
	v_lshl_add_u64 v[174:175], s[46:47], 0, v[164:165]
	s_mov_b32 m0, s37
	ds_read_b128 v[198:201], v188 offset:16384
	ds_read_b128 v[202:205], v188 offset:17408
	ds_read_b128 v[206:209], v188 offset:18432
	ds_read_b128 v[210:213], v188 offset:19456
	ds_read_b128 v[214:217], v188 offset:20480
	ds_read_b128 v[218:221], v188 offset:21504
	ds_read_b128 v[222:225], v188 offset:22528
	ds_read_b128 v[226:229], v188 offset:23552
	global_load_lds_dwordx4 v[174:175], off
	s_add_i32 m0, s37, 0x2000
	s_add_u32 s50, s46, 0x40000
	v_lshl_add_u64 v[176:177], s[46:47], 0, v[166:167]
	s_addc_u32 s51, s47, 0
	s_add_i32 s37, s86, s58
	global_load_lds_dwordx4 v[176:177], off
	v_lshl_add_u64 v[178:179], s[50:51], 0, v[164:165]
	s_mov_b32 m0, s37
	v_cndmask_b32_e64 v162, v196, v192, s[6:7]
	global_load_lds_dwordx4 v[178:179], off
	v_lshl_add_u64 v[178:179], s[50:51], 0, v[166:167]
	s_add_i32 m0, s37, 0x2000
	s_nop 0
	global_load_lds_dwordx4 v[178:179], off
	s_mov_b32 m0, s59
	v_lshl_add_u64 v[178:179], s[48:49], 0, v[162:163]
	global_load_lds_dwordx4 v162, s[48:49]
	v_cndmask_b32_e64 v162, v170, v191, s[6:7]
	s_mov_b32 m0, s60
	v_lshl_add_u64 v[180:181], s[48:49], 0, v[162:163]
	global_load_lds_dwordx4 v162, s[48:49]
	s_waitcnt vmcnt(8)
	s_waitcnt lgkmcnt(0)
	s_barrier
	s_setprio 1
	s_waitcnt lgkmcnt(0)
	v_mfma_f32_16x16x128_f8f6f4 v[94:97], v[18:25], v[198:205], v[94:97]
	v_mfma_f32_16x16x128_f8f6f4 v[86:89], v[26:33], v[198:205], v[86:89]
	v_mfma_f32_16x16x128_f8f6f4 v[78:81], v[18:25], v[206:213], v[78:81]
	v_mfma_f32_16x16x128_f8f6f4 v[70:73], v[26:33], v[206:213], v[70:73]
	v_mfma_f32_16x16x128_f8f6f4 v[62:65], v[18:25], v[214:221], v[62:65]
	v_mfma_f32_16x16x128_f8f6f4 v[54:57], v[26:33], v[214:221], v[54:57]
	v_mfma_f32_16x16x128_f8f6f4 v[46:49], v[18:25], v[222:229], v[46:49]
	v_mfma_f32_16x16x128_f8f6f4 v[38:41], v[26:33], v[222:229], v[38:41]
	s_setprio 0
	s_setprio 1
	v_mfma_f32_16x16x128_f8f6f4 v[90:93], v[2:9], v[198:205], v[90:93]
	v_mfma_f32_16x16x128_f8f6f4 v[82:85], v[10:17], v[198:205], v[82:85]
	v_mfma_f32_16x16x128_f8f6f4 v[74:77], v[2:9], v[206:213], v[74:77]
	v_mfma_f32_16x16x128_f8f6f4 v[66:69], v[10:17], v[206:213], v[66:69]
	v_mfma_f32_16x16x128_f8f6f4 v[58:61], v[2:9], v[214:221], v[58:61]
	v_mfma_f32_16x16x128_f8f6f4 v[50:53], v[10:17], v[214:221], v[50:53]
	v_mfma_f32_16x16x128_f8f6f4 v[42:45], v[2:9], v[222:229], v[42:45]
	v_mfma_f32_16x16x128_f8f6f4 v[34:37], v[10:17], v[222:229], v[34:37]
	s_setprio 0
	s_barrier
	s_add_i32 s37, 0, 0x18000
	s_add_i32 s50, 0, 0x1c000
	v_add_u32_e32 v14, s37, v185
	v_add_u32_e32 v30, s50, v185
	ds_read_b128 v[2:5], v14
	ds_read_b128 v[6:9], v14 offset:1024
	ds_read_b128 v[10:13], v14 offset:2048
	ds_read_b128 v[14:17], v14 offset:3072
	ds_read_b128 v[18:21], v30
	ds_read_b128 v[22:25], v30 offset:1024
	ds_read_b128 v[26:29], v30 offset:2048
	ds_read_b128 v[30:33], v30 offset:3072
	s_mov_b32 m0, s61
	v_cndmask_b32_e64 v162, v168, v190, s[6:7]
	ds_read_b128 v[198:201], v188 offset:32768
	ds_read_b128 v[202:205], v188 offset:33792
	ds_read_b128 v[206:209], v188 offset:34816
	ds_read_b128 v[210:213], v188 offset:35840
	ds_read_b128 v[214:217], v188 offset:36864
	ds_read_b128 v[218:221], v188 offset:37888
	ds_read_b128 v[222:225], v188 offset:38912
	ds_read_b128 v[226:229], v188 offset:39936
	global_load_lds_dwordx4 v162, s[48:49]
	v_cndmask_b32_e64 v162, v172, v193, s[6:7]
	s_mov_b32 m0, s62
	s_nop 0
	global_load_lds_dwordx4 v162, s[48:49]
	s_waitcnt vmcnt(8)
	s_waitcnt lgkmcnt(0)
	s_barrier
	s_setprio 1
	s_waitcnt lgkmcnt(0)
	v_mfma_f32_16x16x128_f8f6f4 v[158:161], v[2:9], v[198:205], v[158:161]
	v_mfma_f32_16x16x128_f8f6f4 v[154:157], v[10:17], v[198:205], v[154:157]
	v_mfma_f32_16x16x128_f8f6f4 v[142:145], v[2:9], v[206:213], v[142:145]
	v_mfma_f32_16x16x128_f8f6f4 v[134:137], v[10:17], v[206:213], v[134:137]
	v_mfma_f32_16x16x128_f8f6f4 v[126:129], v[2:9], v[214:221], v[126:129]
	v_mfma_f32_16x16x128_f8f6f4 v[118:121], v[10:17], v[214:221], v[118:121]
	v_mfma_f32_16x16x128_f8f6f4 v[110:113], v[2:9], v[222:229], v[110:113]
	v_mfma_f32_16x16x128_f8f6f4 v[102:105], v[10:17], v[222:229], v[102:105]
	s_setprio 0
	s_setprio 1
	v_mfma_f32_16x16x128_f8f6f4 v[150:153], v[18:25], v[198:205], v[150:153]
	v_mfma_f32_16x16x128_f8f6f4 v[146:149], v[26:33], v[198:205], v[146:149]
	v_mfma_f32_16x16x128_f8f6f4 v[138:141], v[18:25], v[206:213], v[138:141]
	v_mfma_f32_16x16x128_f8f6f4 v[130:133], v[26:33], v[206:213], v[130:133]
	v_mfma_f32_16x16x128_f8f6f4 v[122:125], v[18:25], v[214:221], v[122:125]
	v_mfma_f32_16x16x128_f8f6f4 v[114:117], v[26:33], v[214:221], v[114:117]
	v_mfma_f32_16x16x128_f8f6f4 v[106:109], v[18:25], v[222:229], v[106:109]
	v_mfma_f32_16x16x128_f8f6f4 v[98:101], v[26:33], v[222:229], v[98:101]
	s_setprio 0
	s_barrier
	s_add_i32 s6, s37, s58
	v_lshl_add_u64 v[174:175], v[174:175], 0, s[16:17]
	s_mov_b32 m0, s6
	ds_read_b128 v[198:201], v188 offset:49152
	ds_read_b128 v[202:205], v188 offset:50176
	ds_read_b128 v[206:209], v188 offset:51200
	ds_read_b128 v[210:213], v188 offset:52224
	ds_read_b128 v[214:217], v188 offset:53248
	ds_read_b128 v[218:221], v188 offset:54272
	ds_read_b128 v[222:225], v188 offset:55296
	ds_read_b128 v[226:229], v188 offset:56320
	global_load_lds_dwordx4 v[174:175], off
	s_add_i32 m0, s6, 0x2000
	s_add_u32 s6, s46, 0x40080
	v_lshl_add_u64 v[174:175], v[176:177], 0, s[16:17]
	s_addc_u32 s7, s47, 0
	s_add_i32 s37, s50, s58
	global_load_lds_dwordx4 v[174:175], off
	v_lshl_add_u64 v[174:175], s[6:7], 0, v[164:165]
	s_mov_b32 m0, s37
	s_nop 0
	global_load_lds_dwordx4 v[174:175], off
	v_lshl_add_u64 v[174:175], s[6:7], 0, v[166:167]
	s_add_i32 m0, s37, 0x2000
	s_nop 0
	global_load_lds_dwordx4 v[174:175], off
	v_lshl_add_u64 v[174:175], v[178:179], 0, s[16:17]
	s_mov_b32 m0, s66
	s_nop 0
	global_load_lds_dwordx4 v[174:175], off
	v_lshl_add_u64 v[174:175], v[180:181], 0, s[16:17]
	s_mov_b32 m0, s67
	s_nop 0
	global_load_lds_dwordx4 v[174:175], off
	s_waitcnt vmcnt(8)
	s_waitcnt lgkmcnt(0)
	s_barrier
	s_setprio 1
	s_waitcnt lgkmcnt(0)
	v_mfma_f32_16x16x128_f8f6f4 v[94:97], v[2:9], v[198:205], v[94:97]
	v_mfma_f32_16x16x128_f8f6f4 v[86:89], v[10:17], v[198:205], v[86:89]
	v_mfma_f32_16x16x128_f8f6f4 v[78:81], v[2:9], v[206:213], v[78:81]
	v_mfma_f32_16x16x128_f8f6f4 v[70:73], v[10:17], v[206:213], v[70:73]
	v_mfma_f32_16x16x128_f8f6f4 v[62:65], v[2:9], v[214:221], v[62:65]
	v_mfma_f32_16x16x128_f8f6f4 v[54:57], v[10:17], v[214:221], v[54:57]
	v_mfma_f32_16x16x128_f8f6f4 v[46:49], v[2:9], v[222:229], v[46:49]
	v_mfma_f32_16x16x128_f8f6f4 v[38:41], v[10:17], v[222:229], v[38:41]
	s_setprio 0
	s_setprio 1
	v_mfma_f32_16x16x128_f8f6f4 v[90:93], v[18:25], v[198:205], v[90:93]
	v_mfma_f32_16x16x128_f8f6f4 v[82:85], v[26:33], v[198:205], v[82:85]
	v_mfma_f32_16x16x128_f8f6f4 v[74:77], v[18:25], v[206:213], v[74:77]
	v_mfma_f32_16x16x128_f8f6f4 v[66:69], v[26:33], v[206:213], v[66:69]
	v_mfma_f32_16x16x128_f8f6f4 v[58:61], v[18:25], v[214:221], v[58:61]
	v_mfma_f32_16x16x128_f8f6f4 v[50:53], v[26:33], v[214:221], v[50:53]
	v_mfma_f32_16x16x128_f8f6f4 v[42:45], v[18:25], v[222:229], v[42:45]
	v_mfma_f32_16x16x128_f8f6f4 v[34:37], v[26:33], v[222:229], v[34:37]
	s_setprio 0
	s_barrier
	s_add_i32 s29, s29, 2
	s_add_u32 s44, s44, 0x100
	s_addc_u32 s45, s45, 0
	s_add_u32 s38, s38, 0x100
	s_addc_u32 s39, s39, 0
	s_cmp_gt_u32 s29, 13
	s_cbranch_scc1 .LBB0_1368
.LBB0_1356:
	s_add_u32 s50, s44, 0x80
	s_addc_u32 s51, s45, 0
	s_add_u32 s37, s44, 0x100
	s_addc_u32 s49, s45, 0
	s_add_u32 s52, s38, 0x100
	s_addc_u32 s53, s39, 0
	s_cmp_eq_u32 s29, 12
	s_cselect_b64 s[6:7], -1, 0
	s_and_b64 s[46:47], s[6:7], exec
	s_cselect_b32 s48, s40, s37
	s_cselect_b32 s49, s41, s49
	s_cselect_b32 s46, s30, s52
	s_cselect_b32 s47, s31, s53
	s_cmp_lg_u32 s29, 12
	s_cbranch_scc1 .Lp9_nofin
	s_andn2_b64 vcc, exec, s[4:5]
	s_cbranch_vccnz .Lp9_nofin
	v_lshl_add_u32 v192, v230, 11, v183
	v_lshl_add_u32 v191, v231, 11, v184
	v_lshl_add_u32 v190, v232, 11, v183
	v_lshl_add_u32 v193, v233, 11, v184
.Lp9_nofin:
	s_cmp_lg_u32 s29, 12
	s_cbranch_scc1 .Lp9_nobias
	s_mov_b32 s98, s36
	s_ashr_i32 s99, s36, 31
	s_lshl_b64 s[98:99], s[98:99], 14
	s_add_u32 s98, s10, s98
	s_addc_u32 s99, s11, s99
	v_lshl_or_b32 v250, s34, 7, v186
	v_ashrrev_i32_e32 v251, 31, v250
	v_lshl_add_u64 v[252:253], v[250:251], 2, s[98:99]
	global_load_dwordx4 v[234:237], v[252:253], off offset:16
	global_load_dwordx4 v[238:241], v[252:253], off
	s_mov_b64 s[98:99], 0x2000
	v_lshl_add_u64 v[250:251], v[252:253], 0, s[98:99]
	global_load_dwordx4 v[242:245], v[250:251], off
	global_load_dwordx4 v[246:249], v[250:251], off offset:16
.Lp9_nobias:
	s_cmp_lg_u32 s29, 10
	s_cbranch_scc1 .LBB0_1355
	s_andn2_b64 vcc, exec, s[4:5]
	v_mov_b32_e32 v192, v196
	v_mov_b32_e32 v191, v170
	v_mov_b32_e32 v190, v168
	v_mov_b32_e32 v193, v172
	s_cbranch_vccnz .LBB0_1355
	v_mov_b32_e32 v2, s27
	ds_read2st64_b32 v[2:3], v2 offset1:1
	v_mov_b32_e32 v230, 0
	v_mov_b32_e32 v231, 0
	v_mov_b32_e32 v232, 0
	v_mov_b32_e32 v233, 0
	s_waitcnt lgkmcnt(0)
	v_sub_u32_e32 v2, v194, v2
	v_lshlrev_b32_e32 v2, 8, v2
	v_add_u32_e32 v4, v2, v1
	v_cmp_lt_i32_e32 vcc, v4, v3
	s_and_saveexec_b64 s[52:53], vcc
	s_cbranch_execz .Lp9_g1
	v_ashrrev_i32_e32 v5, 31, v4
	v_lshl_add_u64 v[4:5], v[4:5], 2, s[42:43]
	global_load_dword v230, v[4:5], off
.Lp9_g1:
	s_or_b64 exec, exec, s[52:53]
	v_add_u32_e32 v4, v2, v182
	v_cmp_lt_i32_e32 vcc, v4, v3
	s_and_saveexec_b64 s[52:53], vcc
	s_cbranch_execz .Lp9_g2
	v_ashrrev_i32_e32 v5, 31, v4
	v_lshl_add_u64 v[4:5], v[4:5], 2, s[42:43]
	global_load_dword v231, v[4:5], off
.Lp9_g2:
	s_or_b64 exec, exec, s[52:53]
	v_or_b32_e32 v2, 0x80, v2
	v_add_u32_e32 v4, v2, v1
	v_cmp_lt_i32_e32 vcc, v4, v3
	s_and_saveexec_b64 s[52:53], vcc
	s_cbranch_execz .Lp9_g3
	v_ashrrev_i32_e32 v5, 31, v4
	v_lshl_add_u64 v[4:5], v[4:5], 2, s[42:43]
	global_load_dword v232, v[4:5], off
.Lp9_g3:
	s_or_b64 exec, exec, s[52:53]
	v_add_u32_e32 v2, v2, v182
	v_cmp_lt_i32_e32 vcc, v2, v3
	s_and_saveexec_b64 s[52:53], vcc
	s_cbranch_execz .Lp9_g4
	v_ashrrev_i32_e32 v3, 31, v2
	v_lshl_add_u64 v[2:3], v[2:3], 2, s[42:43]
	global_load_dword v233, v[2:3], off
.Lp9_g4:
	s_or_b64 exec, exec, s[52:53]
	s_branch .LBB0_1355

.LBB0_1370:
	s_ashr_i32 s37, s36, 31
	s_lshl_b64 s[6:7], s[36:37], 14
	v_lshl_or_b32 v22, s34, 7, v186
	s_add_u32 s6, s10, s6
	s_addc_u32 s7, s11, s7
	v_ashrrev_i32_e32 v23, 31, v22
	s_nop 15
	s_nop 15
	s_mov_b64 s[6:7], 0x2000
	v_lshl_add_u32 v18, v195, 8, v171
	v_or_b32_e32 v24, 16, v18
	v_or_b32_e32 v26, 32, v18
	v_or_b32_e32 v28, 48, v18
	v_ashrrev_i32_e32 v19, 31, v18
	v_ashrrev_i32_e32 v25, 31, v24
	v_ashrrev_i32_e32 v27, 31, v26
	v_ashrrev_i32_e32 v29, 31, v28
	v_lshlrev_b64 v[18:19], 11, v[18:19]
	v_lshlrev_b64 v[24:25], 11, v[24:25]
	v_lshlrev_b64 v[26:27], 11, v[26:27]
	v_lshlrev_b64 v[28:29], 11, v[28:29]
	v_lshl_add_u64 v[18:19], s[14:15], 0, v[18:19]
	v_lshl_add_u64 v[24:25], s[14:15], 0, v[24:25]
	v_lshl_add_u64 v[26:27], s[14:15], 0, v[26:27]
	v_lshl_add_u64 v[28:29], s[14:15], 0, v[28:29]
	v_lshl_add_u64 v[18:19], v[18:19], 0, v[22:23]
	v_lshl_add_u64 v[24:25], v[24:25], 0, v[22:23]
	v_lshl_add_u64 v[26:27], v[26:27], 0, v[22:23]
	v_lshl_add_u64 v[22:23], v[28:29], 0, v[22:23]
	v_mov_b32_e32 v20, v163
	v_mov_b32_e32 v21, v163
	s_mov_b32 s6, 0x40000
	v_mov_b64_e32 v[6:7], v[234:235]
	v_mov_b64_e32 v[8:9], v[236:237]
	v_mov_b64_e32 v[14:15], v[238:239]
	v_mov_b64_e32 v[16:17], v[240:241]
	v_mov_b64_e32 v[10:11], v[242:243]
	v_mov_b64_e32 v[12:13], v[244:245]
	v_mov_b64_e32 v[2:3], v[246:247]
	v_mov_b64_e32 v[4:5], v[248:249]
	v_pk_fma_f32 v[32:33], v[154:155], s[22:23], v[6:7] op_sel_hi:[1,0,1]
	v_pk_fma_f32 v[28:29], v[158:159], s[22:23], v[14:15] op_sel_hi:[1,0,1]
	v_pk_fma_f32 v[154:155], v[156:157], s[22:23], v[8:9] op_sel_hi:[1,0,1]
	v_min_f32_e32 v28, 0x40e00000, v28
	v_min_f32_e32 v29, 0x40e00000, v29
	v_min_f32_e32 v32, 0x40e00000, v32
	v_min_f32_e32 v33, 0x40e00000, v33
	v_pk_mul_f32 v[156:157], v[28:29], s[24:25] op_sel_hi:[1,0]
	v_pk_fma_f32 v[30:31], v[160:161], s[22:23], v[16:17] op_sel_hi:[1,0,1]
	v_pk_mul_f32 v[160:161], v[32:33], s[24:25] op_sel_hi:[1,0]
	v_exp_f32_e32 v156, v156
	v_exp_f32_e32 v157, v157
	v_exp_f32_e32 v160, v160
	v_exp_f32_e32 v161, v161
	v_min_f32_e32 v30, 0x40e00000, v30
	v_min_f32_e32 v31, 0x40e00000, v31
	v_min_f32_e32 v154, 0x40e00000, v154
	v_min_f32_e32 v155, 0x40e00000, v155
	v_pk_mul_f32 v[158:159], v[30:31], s[24:25] op_sel_hi:[1,0]
	v_pk_mul_f32 v[168:169], v[154:155], s[24:25] op_sel_hi:[1,0]
	v_exp_f32_e32 v158, v158
	v_exp_f32_e32 v159, v159
	v_pk_add_f32 v[156:157], v[156:157], 1.0 op_sel_hi:[1,0]
	v_exp_f32_e32 v168, v168
	v_exp_f32_e32 v169, v169
	v_pk_add_f32 v[160:161], v[160:161], 1.0 op_sel_hi:[1,0]
	v_rcp_f32_e32 v156, v156
	v_rcp_f32_e32 v157, v157
	v_rcp_f32_e32 v160, v160
	v_rcp_f32_e32 v161, v161
	v_pk_fma_f32 v[150:151], v[150:151], s[22:23], v[10:11] op_sel_hi:[1,0,1]
	v_pk_fma_f32 v[146:147], v[146:147], s[22:23], v[2:3] op_sel_hi:[1,0,1]
	v_med3_f32 v150, v150, s87, v189
	v_med3_f32 v151, v151, s87, v189
	v_pk_add_f32 v[158:159], v[158:159], 1.0 op_sel_hi:[1,0]
	v_med3_f32 v146, v146, s87, v189
	v_med3_f32 v147, v147, s87, v189
	v_pk_add_f32 v[150:151], v[150:151], 1.0 op_sel_hi:[1,0]
	v_pk_add_f32 v[168:169], v[168:169], 1.0 op_sel_hi:[1,0]
	v_rcp_f32_e32 v158, v158
	v_rcp_f32_e32 v159, v159
	v_pk_mul_f32 v[28:29], v[28:29], v[156:157]
	v_pk_add_f32 v[146:147], v[146:147], 1.0 op_sel_hi:[1,0]
	v_rcp_f32_e32 v168, v168
	v_rcp_f32_e32 v169, v169
	v_pk_mul_f32 v[32:33], v[32:33], v[160:161]
	v_pk_mul_f32 v[28:29], v[150:151], v[28:29]
	v_pk_fma_f32 v[152:153], v[152:153], s[22:23], v[12:13] op_sel_hi:[1,0,1]
	v_pk_mul_f32 v[32:33], v[146:147], v[32:33]
	v_cvt_pk_fp8_f32 v20, v28, v29
	v_pk_fma_f32 v[148:149], v[148:149], s[22:23], v[4:5] op_sel_hi:[1,0,1]
	v_med3_f32 v152, v152, s87, v189
	v_med3_f32 v153, v153, s87, v189
	v_cvt_pk_fp8_f32 v21, v32, v33
	v_med3_f32 v148, v148, s87, v189
	v_med3_f32 v149, v149, s87, v189
	v_pk_add_f32 v[152:153], v[152:153], 1.0 op_sel_hi:[1,0]
	v_pk_mul_f32 v[30:31], v[30:31], v[158:159]
	v_pk_fma_f32 v[142:143], v[142:143], s[22:23], v[14:15] op_sel_hi:[1,0,1]
	v_pk_add_f32 v[148:149], v[148:149], 1.0 op_sel_hi:[1,0]
	v_pk_mul_f32 v[154:155], v[154:155], v[168:169]
	v_pk_mul_f32 v[28:29], v[152:153], v[30:31]
	v_pk_mul_f32 v[30:31], v[148:149], v[154:155]
	v_cvt_pk_fp8_f32 v20, v28, v29 op_sel:[0,0,1]
	v_min_f32_e32 v28, 0x40e00000, v142
	v_min_f32_e32 v29, 0x40e00000, v143
	v_cvt_pk_fp8_f32 v21, v30, v31 op_sel:[0,0,1]
	v_pk_mul_f32 v[30:31], v[28:29], s[24:25] op_sel_hi:[1,0]
	v_pk_fma_f32 v[32:33], v[138:139], s[22:23], v[10:11] op_sel_hi:[1,0,1]
	v_exp_f32_e32 v30, v30
	v_exp_f32_e32 v31, v31
	v_pk_fma_f32 v[138:139], v[144:145], s[22:23], v[16:17] op_sel_hi:[1,0,1]
	v_med3_f32 v32, v32, s87, v189
	v_min_f32_e32 v138, 0x40e00000, v138
	v_pk_add_f32 v[30:31], v[30:31], 1.0 op_sel_hi:[1,0]
	v_min_f32_e32 v139, 0x40e00000, v139
	v_rcp_f32_e32 v30, v30
	v_rcp_f32_e32 v31, v31
	v_pk_mul_f32 v[142:143], v[138:139], s[24:25] op_sel_hi:[1,0]
	v_med3_f32 v33, v33, s87, v189
	v_exp_f32_e32 v142, v142
	v_exp_f32_e32 v143, v143
	v_pk_mul_f32 v[28:29], v[28:29], v[30:31]
	v_pk_add_f32 v[30:31], v[32:33], 1.0 op_sel_hi:[1,0]
	v_pk_fma_f32 v[32:33], v[140:141], s[22:23], v[12:13] op_sel_hi:[1,0,1]
	v_pk_mul_f32 v[30:31], v[30:31], v[28:29]
	v_pk_add_f32 v[28:29], v[142:143], 1.0 op_sel_hi:[1,0]
	v_med3_f32 v32, v32, s87, v189
	v_rcp_f32_e32 v28, v28
	v_rcp_f32_e32 v29, v29
	v_med3_f32 v33, v33, s87, v189
	v_pk_add_f32 v[32:33], v[32:33], 1.0 op_sel_hi:[1,0]
	v_pk_fma_f32 v[136:137], v[136:137], s[22:23], v[8:9] op_sel_hi:[1,0,1]
	v_pk_mul_f32 v[28:29], v[138:139], v[28:29]
	v_min_f32_e32 v136, 0x40e00000, v136
	v_pk_mul_f32 v[32:33], v[32:33], v[28:29]
	v_pk_fma_f32 v[28:29], v[134:135], s[22:23], v[6:7] op_sel_hi:[1,0,1]
	v_min_f32_e32 v137, 0x40e00000, v137
	v_min_f32_e32 v28, 0x40e00000, v28
	v_min_f32_e32 v29, 0x40e00000, v29
	v_pk_mul_f32 v[134:135], v[28:29], s[24:25] op_sel_hi:[1,0]
	v_pk_mul_f32 v[138:139], v[136:137], s[24:25] op_sel_hi:[1,0]
	v_exp_f32_e32 v134, v134
	v_exp_f32_e32 v135, v135
	v_exp_f32_e32 v138, v138
	v_exp_f32_e32 v139, v139
	v_pk_fma_f32 v[130:131], v[130:131], s[22:23], v[2:3] op_sel_hi:[1,0,1]
	v_pk_add_f32 v[134:135], v[134:135], 1.0 op_sel_hi:[1,0]
	v_med3_f32 v130, v130, s87, v189
	v_rcp_f32_e32 v134, v134
	v_rcp_f32_e32 v135, v135
	v_med3_f32 v131, v131, s87, v189
	v_pk_add_f32 v[130:131], v[130:131], 1.0 op_sel_hi:[1,0]
	v_pk_fma_f32 v[132:133], v[132:133], s[22:23], v[4:5] op_sel_hi:[1,0,1]
	v_pk_mul_f32 v[28:29], v[28:29], v[134:135]
	v_med3_f32 v132, v132, s87, v189
	v_pk_mul_f32 v[130:131], v[130:131], v[28:29]
	v_pk_add_f32 v[28:29], v[138:139], 1.0 op_sel_hi:[1,0]
	v_med3_f32 v133, v133, s87, v189
	v_rcp_f32_e32 v28, v28
	v_rcp_f32_e32 v29, v29
	v_pk_fma_f32 v[122:123], v[122:123], s[22:23], v[10:11] op_sel_hi:[1,0,1]
	v_pk_fma_f32 v[118:119], v[118:119], s[22:23], v[6:7] op_sel_hi:[1,0,1]
	v_med3_f32 v122, v122, s87, v189
	v_pk_mul_f32 v[134:135], v[136:137], v[28:29]
	v_mov_b32_e32 v29, v163
	v_cvt_pk_fp8_f32 v29, v130, v131
	v_mov_b32_e32 v28, v163
	v_cvt_pk_fp8_f32 v28, v30, v31
	v_pk_add_f32 v[30:31], v[132:133], 1.0 op_sel_hi:[1,0]
	v_med3_f32 v123, v123, s87, v189
	v_pk_mul_f32 v[30:31], v[30:31], v[134:135]
	v_cvt_pk_fp8_f32 v28, v32, v33 op_sel:[0,0,1]
	v_cvt_pk_fp8_f32 v29, v30, v31 op_sel:[0,0,1]
	v_pk_fma_f32 v[30:31], v[126:127], s[22:23], v[14:15] op_sel_hi:[1,0,1]
	v_pk_fma_f32 v[126:127], v[128:129], s[22:23], v[16:17] op_sel_hi:[1,0,1]
	v_min_f32_e32 v30, 0x40e00000, v30
	v_min_f32_e32 v31, 0x40e00000, v31
	v_pk_mul_f32 v[32:33], v[30:31], s[24:25] op_sel_hi:[1,0]
	v_min_f32_e32 v126, 0x40e00000, v126
	v_exp_f32_e32 v32, v32
	v_exp_f32_e32 v33, v33
	v_min_f32_e32 v127, 0x40e00000, v127
	v_pk_mul_f32 v[128:129], v[126:127], s[24:25] op_sel_hi:[1,0]
	v_min_f32_e32 v118, 0x40e00000, v118
	v_pk_add_f32 v[32:33], v[32:33], 1.0 op_sel_hi:[1,0]
	v_exp_f32_e32 v128, v128
	v_rcp_f32_e32 v32, v32
	v_rcp_f32_e32 v33, v33
	v_exp_f32_e32 v129, v129
	v_min_f32_e32 v119, 0x40e00000, v119
	v_pk_fma_f32 v[120:121], v[120:121], s[22:23], v[8:9] op_sel_hi:[1,0,1]
	v_pk_mul_f32 v[30:31], v[30:31], v[32:33]
	v_pk_add_f32 v[32:33], v[122:123], 1.0 op_sel_hi:[1,0]
	v_pk_fma_f32 v[122:123], v[124:125], s[22:23], v[12:13] op_sel_hi:[1,0,1]
	v_pk_mul_f32 v[30:31], v[32:33], v[30:31]
	v_pk_add_f32 v[32:33], v[128:129], 1.0 op_sel_hi:[1,0]
	v_med3_f32 v122, v122, s87, v189
	v_rcp_f32_e32 v32, v32
	v_rcp_f32_e32 v33, v33
	v_med3_f32 v123, v123, s87, v189
	v_pk_add_f32 v[122:123], v[122:123], 1.0 op_sel_hi:[1,0]
	v_min_f32_e32 v120, 0x40e00000, v120
	v_pk_mul_f32 v[32:33], v[126:127], v[32:33]
	v_min_f32_e32 v121, 0x40e00000, v121
	v_pk_mul_f32 v[32:33], v[122:123], v[32:33]
	v_pk_mul_f32 v[122:123], v[118:119], s[24:25] op_sel_hi:[1,0]
	v_pk_mul_f32 v[124:125], v[120:121], s[24:25] op_sel_hi:[1,0]
	v_exp_f32_e32 v122, v122
	v_exp_f32_e32 v123, v123
	v_exp_f32_e32 v124, v124
	v_exp_f32_e32 v125, v125
	v_pk_fma_f32 v[114:115], v[114:115], s[22:23], v[2:3] op_sel_hi:[1,0,1]
	v_pk_add_f32 v[122:123], v[122:123], 1.0 op_sel_hi:[1,0]
	v_med3_f32 v114, v114, s87, v189
	v_rcp_f32_e32 v122, v122
	v_rcp_f32_e32 v123, v123
	v_med3_f32 v115, v115, s87, v189
	v_pk_add_f32 v[114:115], v[114:115], 1.0 op_sel_hi:[1,0]
	v_pk_fma_f32 v[116:117], v[116:117], s[22:23], v[4:5] op_sel_hi:[1,0,1]
	v_pk_mul_f32 v[118:119], v[118:119], v[122:123]
	v_med3_f32 v116, v116, s87, v189
	v_pk_mul_f32 v[114:115], v[114:115], v[118:119]
	v_pk_add_f32 v[118:119], v[124:125], 1.0 op_sel_hi:[1,0]
	v_med3_f32 v117, v117, s87, v189
	v_rcp_f32_e32 v118, v118
	v_rcp_f32_e32 v119, v119
	v_pk_fma_f32 v[106:107], v[106:107], s[22:23], v[10:11] op_sel_hi:[1,0,1]
	v_pk_fma_f32 v[102:103], v[102:103], s[22:23], v[6:7] op_sel_hi:[1,0,1]
	v_med3_f32 v106, v106, s87, v189
	v_pk_mul_f32 v[118:119], v[120:121], v[118:119]
	v_mov_b32_e32 v121, v163
	v_cvt_pk_fp8_f32 v121, v114, v115
	v_mov_b32_e32 v120, v163
	v_cvt_pk_fp8_f32 v120, v30, v31
	v_pk_add_f32 v[30:31], v[116:117], 1.0 op_sel_hi:[1,0]
	v_med3_f32 v107, v107, s87, v189
	v_pk_mul_f32 v[30:31], v[30:31], v[118:119]
	v_cvt_pk_fp8_f32 v120, v32, v33 op_sel:[0,0,1]
	v_cvt_pk_fp8_f32 v121, v30, v31 op_sel:[0,0,1]
	v_pk_fma_f32 v[30:31], v[110:111], s[22:23], v[14:15] op_sel_hi:[1,0,1]
	v_pk_fma_f32 v[110:111], v[112:113], s[22:23], v[16:17] op_sel_hi:[1,0,1]
	v_min_f32_e32 v30, 0x40e00000, v30
	v_min_f32_e32 v31, 0x40e00000, v31
	v_pk_mul_f32 v[32:33], v[30:31], s[24:25] op_sel_hi:[1,0]
	v_min_f32_e32 v110, 0x40e00000, v110
	v_exp_f32_e32 v32, v32
	v_exp_f32_e32 v33, v33
	v_min_f32_e32 v111, 0x40e00000, v111
	v_pk_mul_f32 v[112:113], v[110:111], s[24:25] op_sel_hi:[1,0]
	v_min_f32_e32 v102, 0x40e00000, v102
	v_pk_add_f32 v[32:33], v[32:33], 1.0 op_sel_hi:[1,0]
	v_exp_f32_e32 v112, v112
	v_rcp_f32_e32 v32, v32
	v_rcp_f32_e32 v33, v33
	v_exp_f32_e32 v113, v113
	v_min_f32_e32 v103, 0x40e00000, v103
	v_pk_fma_f32 v[104:105], v[104:105], s[22:23], v[8:9] op_sel_hi:[1,0,1]
	v_pk_mul_f32 v[30:31], v[30:31], v[32:33]
	v_pk_add_f32 v[32:33], v[106:107], 1.0 op_sel_hi:[1,0]
	v_pk_fma_f32 v[106:107], v[108:109], s[22:23], v[12:13] op_sel_hi:[1,0,1]
	v_pk_mul_f32 v[30:31], v[32:33], v[30:31]
	v_pk_add_f32 v[32:33], v[112:113], 1.0 op_sel_hi:[1,0]
	v_med3_f32 v106, v106, s87, v189
	v_rcp_f32_e32 v32, v32
	v_rcp_f32_e32 v33, v33
	v_med3_f32 v107, v107, s87, v189
	v_pk_add_f32 v[106:107], v[106:107], 1.0 op_sel_hi:[1,0]
	v_min_f32_e32 v104, 0x40e00000, v104
	v_pk_mul_f32 v[32:33], v[110:111], v[32:33]
	v_min_f32_e32 v105, 0x40e00000, v105
	v_pk_mul_f32 v[32:33], v[106:107], v[32:33]
	v_pk_mul_f32 v[106:107], v[102:103], s[24:25] op_sel_hi:[1,0]
	v_pk_mul_f32 v[108:109], v[104:105], s[24:25] op_sel_hi:[1,0]
	v_exp_f32_e32 v106, v106
	v_exp_f32_e32 v107, v107
	v_exp_f32_e32 v108, v108
	v_exp_f32_e32 v109, v109
	v_pk_fma_f32 v[98:99], v[98:99], s[22:23], v[2:3] op_sel_hi:[1,0,1]
	v_pk_add_f32 v[106:107], v[106:107], 1.0 op_sel_hi:[1,0]
	v_med3_f32 v98, v98, s87, v189
	v_rcp_f32_e32 v106, v106
	v_rcp_f32_e32 v107, v107
	v_med3_f32 v99, v99, s87, v189
	v_pk_add_f32 v[98:99], v[98:99], 1.0 op_sel_hi:[1,0]
	v_pk_fma_f32 v[100:101], v[100:101], s[22:23], v[4:5] op_sel_hi:[1,0,1]
	v_pk_mul_f32 v[102:103], v[102:103], v[106:107]
	v_med3_f32 v100, v100, s87, v189
	v_pk_mul_f32 v[98:99], v[98:99], v[102:103]
	v_pk_add_f32 v[102:103], v[108:109], 1.0 op_sel_hi:[1,0]
	v_med3_f32 v101, v101, s87, v189
	v_rcp_f32_e32 v102, v102
	v_rcp_f32_e32 v103, v103
	s_nop 0
	v_pk_mul_f32 v[102:103], v[104:105], v[102:103]
	v_mov_b32_e32 v104, v163
	v_mov_b32_e32 v105, v163
	v_cvt_pk_fp8_f32 v104, v30, v31
	v_cvt_pk_fp8_f32 v105, v98, v99
	v_pk_add_f32 v[30:31], v[100:101], 1.0 op_sel_hi:[1,0]
	v_cvt_pk_fp8_f32 v104, v32, v33 op_sel:[0,0,1]
	v_pk_mul_f32 v[30:31], v[30:31], v[102:103]
	s_nop 0
	v_cvt_pk_fp8_f32 v105, v30, v31 op_sel:[0,0,1]
	global_store_dwordx2 v[18:19], v[20:21], off nt
	global_store_dwordx2 v[24:25], v[28:29], off nt
	global_store_dwordx2 v[26:27], v[120:121], off nt
	global_store_dwordx2 v[22:23], v[104:105], off nt
	v_pk_fma_f32 v[20:21], v[94:95], s[22:23], v[14:15] op_sel_hi:[1,0,1]
	v_pk_fma_f32 v[26:27], v[96:97], s[22:23], v[16:17] op_sel_hi:[1,0,1]
	v_min_f32_e32 v20, 0x40e00000, v20
	v_min_f32_e32 v21, 0x40e00000, v21
	v_pk_mul_f32 v[22:23], v[20:21], s[24:25] op_sel_hi:[1,0]
	v_min_f32_e32 v26, 0x40e00000, v26
	v_exp_f32_e32 v22, v22
	v_exp_f32_e32 v23, v23
	v_min_f32_e32 v27, 0x40e00000, v27
	v_pk_mul_f32 v[28:29], v[26:27], s[24:25] op_sel_hi:[1,0]
	v_pk_fma_f32 v[24:25], v[90:91], s[22:23], v[10:11] op_sel_hi:[1,0,1]
	v_pk_add_f32 v[22:23], v[22:23], 1.0 op_sel_hi:[1,0]
	v_exp_f32_e32 v28, v28
	v_rcp_f32_e32 v22, v22
	v_rcp_f32_e32 v23, v23
	v_exp_f32_e32 v29, v29
	v_med3_f32 v24, v24, s87, v189
	v_med3_f32 v25, v25, s87, v189
	v_pk_mul_f32 v[20:21], v[20:21], v[22:23]
	v_pk_add_f32 v[22:23], v[24:25], 1.0 op_sel_hi:[1,0]
	v_pk_fma_f32 v[24:25], v[92:93], s[22:23], v[12:13] op_sel_hi:[1,0,1]
	v_pk_mul_f32 v[20:21], v[22:23], v[20:21]
	v_pk_add_f32 v[22:23], v[28:29], 1.0 op_sel_hi:[1,0]
	v_med3_f32 v24, v24, s87, v189
	v_rcp_f32_e32 v22, v22
	v_rcp_f32_e32 v23, v23
	v_med3_f32 v25, v25, s87, v189
	v_pk_add_f32 v[24:25], v[24:25], 1.0 op_sel_hi:[1,0]
	v_pk_fma_f32 v[30:31], v[88:89], s[22:23], v[8:9] op_sel_hi:[1,0,1]
	v_pk_mul_f32 v[22:23], v[26:27], v[22:23]
	v_min_f32_e32 v30, 0x40e00000, v30
	v_pk_mul_f32 v[22:23], v[24:25], v[22:23]
	v_pk_fma_f32 v[24:25], v[86:87], s[22:23], v[6:7] op_sel_hi:[1,0,1]
	v_min_f32_e32 v31, 0x40e00000, v31
	v_min_f32_e32 v24, 0x40e00000, v24
	v_min_f32_e32 v25, 0x40e00000, v25
	v_pk_mul_f32 v[26:27], v[24:25], s[24:25] op_sel_hi:[1,0]
	v_pk_mul_f32 v[32:33], v[30:31], s[24:25] op_sel_hi:[1,0]
	v_exp_f32_e32 v26, v26
	v_exp_f32_e32 v27, v27
	v_exp_f32_e32 v32, v32
	v_exp_f32_e32 v33, v33
	v_pk_fma_f32 v[28:29], v[82:83], s[22:23], v[2:3] op_sel_hi:[1,0,1]
	v_pk_add_f32 v[26:27], v[26:27], 1.0 op_sel_hi:[1,0]
	v_med3_f32 v28, v28, s87, v189
	v_rcp_f32_e32 v26, v26
	v_rcp_f32_e32 v27, v27
	v_med3_f32 v29, v29, s87, v189
	v_pk_mul_f32 v[24:25], v[24:25], v[26:27]
	v_pk_add_f32 v[26:27], v[28:29], 1.0 op_sel_hi:[1,0]
	v_pk_fma_f32 v[28:29], v[84:85], s[22:23], v[4:5] op_sel_hi:[1,0,1]
	v_pk_mul_f32 v[24:25], v[26:27], v[24:25]
	v_pk_add_f32 v[26:27], v[32:33], 1.0 op_sel_hi:[1,0]
	v_med3_f32 v28, v28, s87, v189
	v_rcp_f32_e32 v26, v26
	v_rcp_f32_e32 v27, v27
	v_med3_f32 v29, v29, s87, v189
	v_pk_mul_f32 v[26:27], v[30:31], v[26:27]
	v_mov_b32_e32 v30, v163
	v_mov_b32_e32 v31, v163
	v_cvt_pk_fp8_f32 v30, v20, v21
	v_cvt_pk_fp8_f32 v31, v24, v25
	v_pk_add_f32 v[20:21], v[28:29], 1.0 op_sel_hi:[1,0]
	v_pk_fma_f32 v[24:25], v[74:75], s[22:23], v[10:11] op_sel_hi:[1,0,1]
	v_pk_mul_f32 v[20:21], v[20:21], v[26:27]
	v_cvt_pk_fp8_f32 v30, v22, v23 op_sel:[0,0,1]
	v_cvt_pk_fp8_f32 v31, v20, v21 op_sel:[0,0,1]
	v_add_co_u32_e32 v20, vcc, s6, v18
	v_pk_fma_f32 v[26:27], v[80:81], s[22:23], v[16:17] op_sel_hi:[1,0,1]
	s_nop 0
	v_addc_co_u32_e32 v21, vcc, 0, v19, vcc
	global_store_dwordx2 v[20:21], v[30:31], off nt
	v_pk_fma_f32 v[20:21], v[78:79], s[22:23], v[14:15] op_sel_hi:[1,0,1]
	v_min_f32_e32 v26, 0x40e00000, v26
	v_min_f32_e32 v20, 0x40e00000, v20
	v_min_f32_e32 v21, 0x40e00000, v21
	v_pk_mul_f32 v[22:23], v[20:21], s[24:25] op_sel_hi:[1,0]
	v_min_f32_e32 v27, 0x40e00000, v27
	v_exp_f32_e32 v22, v22
	v_exp_f32_e32 v23, v23
	v_pk_mul_f32 v[28:29], v[26:27], s[24:25] op_sel_hi:[1,0]
	v_med3_f32 v24, v24, s87, v189
	v_exp_f32_e32 v28, v28
	v_pk_add_f32 v[22:23], v[22:23], 1.0 op_sel_hi:[1,0]
	v_exp_f32_e32 v29, v29
	v_rcp_f32_e32 v22, v22
	v_rcp_f32_e32 v23, v23
	v_med3_f32 v25, v25, s87, v189
	v_pk_fma_f32 v[30:31], v[72:73], s[22:23], v[8:9] op_sel_hi:[1,0,1]
	s_mov_b32 s6, 0x48000
	v_pk_mul_f32 v[20:21], v[20:21], v[22:23]
	v_pk_add_f32 v[22:23], v[24:25], 1.0 op_sel_hi:[1,0]
	v_pk_fma_f32 v[24:25], v[76:77], s[22:23], v[12:13] op_sel_hi:[1,0,1]
	v_pk_mul_f32 v[20:21], v[22:23], v[20:21]
	v_pk_add_f32 v[22:23], v[28:29], 1.0 op_sel_hi:[1,0]
	v_med3_f32 v24, v24, s87, v189
	v_rcp_f32_e32 v22, v22
	v_rcp_f32_e32 v23, v23
	v_med3_f32 v25, v25, s87, v189
	v_pk_add_f32 v[24:25], v[24:25], 1.0 op_sel_hi:[1,0]
	v_min_f32_e32 v30, 0x40e00000, v30
	v_pk_mul_f32 v[22:23], v[26:27], v[22:23]
	v_min_f32_e32 v31, 0x40e00000, v31
	v_pk_mul_f32 v[22:23], v[24:25], v[22:23]
	v_pk_fma_f32 v[24:25], v[70:71], s[22:23], v[6:7] op_sel_hi:[1,0,1]
	v_pk_mul_f32 v[32:33], v[30:31], s[24:25] op_sel_hi:[1,0]
	v_min_f32_e32 v24, 0x40e00000, v24
	v_min_f32_e32 v25, 0x40e00000, v25
	v_pk_mul_f32 v[26:27], v[24:25], s[24:25] op_sel_hi:[1,0]
	v_exp_f32_e32 v32, v32
	v_exp_f32_e32 v26, v26
	v_exp_f32_e32 v27, v27
	v_exp_f32_e32 v33, v33
	v_pk_fma_f32 v[28:29], v[66:67], s[22:23], v[2:3] op_sel_hi:[1,0,1]
	v_pk_add_f32 v[26:27], v[26:27], 1.0 op_sel_hi:[1,0]
	s_nop 0
	v_rcp_f32_e32 v26, v26
	v_rcp_f32_e32 v27, v27
	v_med3_f32 v28, v28, s87, v189
	v_med3_f32 v29, v29, s87, v189
	v_pk_mul_f32 v[24:25], v[24:25], v[26:27]
	v_pk_add_f32 v[26:27], v[28:29], 1.0 op_sel_hi:[1,0]
	v_pk_fma_f32 v[28:29], v[68:69], s[22:23], v[4:5] op_sel_hi:[1,0,1]
	v_pk_mul_f32 v[24:25], v[26:27], v[24:25]
	v_pk_add_f32 v[26:27], v[32:33], 1.0 op_sel_hi:[1,0]
	v_med3_f32 v28, v28, s87, v189
	v_rcp_f32_e32 v26, v26
	v_rcp_f32_e32 v27, v27
	v_med3_f32 v29, v29, s87, v189
	v_pk_mul_f32 v[26:27], v[30:31], v[26:27]
	v_mov_b32_e32 v30, v163
	v_mov_b32_e32 v31, v163
	v_cvt_pk_fp8_f32 v30, v20, v21
	v_cvt_pk_fp8_f32 v31, v24, v25
	v_pk_add_f32 v[20:21], v[28:29], 1.0 op_sel_hi:[1,0]
	v_pk_fma_f32 v[24:25], v[58:59], s[22:23], v[10:11] op_sel_hi:[1,0,1]
	v_pk_mul_f32 v[20:21], v[20:21], v[26:27]
	v_cvt_pk_fp8_f32 v30, v22, v23 op_sel:[0,0,1]
	v_cvt_pk_fp8_f32 v31, v20, v21 op_sel:[0,0,1]
	v_add_co_u32_e32 v20, vcc, s6, v18
	v_pk_fma_f32 v[26:27], v[64:65], s[22:23], v[16:17] op_sel_hi:[1,0,1]
	s_nop 0
	v_addc_co_u32_e32 v21, vcc, 0, v19, vcc
	global_store_dwordx2 v[20:21], v[30:31], off nt
	v_pk_fma_f32 v[20:21], v[62:63], s[22:23], v[14:15] op_sel_hi:[1,0,1]
	v_min_f32_e32 v26, 0x40e00000, v26
	v_min_f32_e32 v20, 0x40e00000, v20
	v_min_f32_e32 v21, 0x40e00000, v21
	v_pk_mul_f32 v[22:23], v[20:21], s[24:25] op_sel_hi:[1,0]
	v_min_f32_e32 v27, 0x40e00000, v27
	v_exp_f32_e32 v22, v22
	v_exp_f32_e32 v23, v23
	v_pk_mul_f32 v[28:29], v[26:27], s[24:25] op_sel_hi:[1,0]
	v_med3_f32 v24, v24, s87, v189
	v_exp_f32_e32 v28, v28
	v_pk_add_f32 v[22:23], v[22:23], 1.0 op_sel_hi:[1,0]
	v_exp_f32_e32 v29, v29
	v_rcp_f32_e32 v22, v22
	v_rcp_f32_e32 v23, v23
	v_med3_f32 v25, v25, s87, v189
	v_pk_fma_f32 v[30:31], v[56:57], s[22:23], v[8:9] op_sel_hi:[1,0,1]
	s_mov_b32 s6, 0x50000
	v_pk_mul_f32 v[20:21], v[20:21], v[22:23]
	v_pk_add_f32 v[22:23], v[24:25], 1.0 op_sel_hi:[1,0]
	v_pk_fma_f32 v[24:25], v[60:61], s[22:23], v[12:13] op_sel_hi:[1,0,1]
	v_pk_mul_f32 v[20:21], v[22:23], v[20:21]
	v_pk_add_f32 v[22:23], v[28:29], 1.0 op_sel_hi:[1,0]
	v_med3_f32 v24, v24, s87, v189
	v_rcp_f32_e32 v22, v22
	v_rcp_f32_e32 v23, v23
	v_med3_f32 v25, v25, s87, v189
	v_pk_add_f32 v[24:25], v[24:25], 1.0 op_sel_hi:[1,0]
	v_min_f32_e32 v30, 0x40e00000, v30
	v_pk_mul_f32 v[22:23], v[26:27], v[22:23]
	v_min_f32_e32 v31, 0x40e00000, v31
	v_pk_mul_f32 v[22:23], v[24:25], v[22:23]
	v_pk_fma_f32 v[24:25], v[54:55], s[22:23], v[6:7] op_sel_hi:[1,0,1]
	v_pk_mul_f32 v[32:33], v[30:31], s[24:25] op_sel_hi:[1,0]
	v_min_f32_e32 v24, 0x40e00000, v24
	v_min_f32_e32 v25, 0x40e00000, v25
	v_pk_mul_f32 v[26:27], v[24:25], s[24:25] op_sel_hi:[1,0]
	v_exp_f32_e32 v32, v32
	v_exp_f32_e32 v26, v26
	v_exp_f32_e32 v27, v27
	v_exp_f32_e32 v33, v33
	v_pk_fma_f32 v[28:29], v[50:51], s[22:23], v[2:3] op_sel_hi:[1,0,1]
	v_pk_fma_f32 v[14:15], v[46:47], s[22:23], v[14:15] op_sel_hi:[1,0,1]
	v_pk_add_f32 v[26:27], v[26:27], 1.0 op_sel_hi:[1,0]
	v_med3_f32 v28, v28, s87, v189
	v_rcp_f32_e32 v26, v26
	v_rcp_f32_e32 v27, v27
	v_med3_f32 v29, v29, s87, v189
	v_min_f32_e32 v14, 0x40e00000, v14
	v_min_f32_e32 v15, 0x40e00000, v15
	v_pk_mul_f32 v[24:25], v[24:25], v[26:27]
	v_pk_add_f32 v[26:27], v[28:29], 1.0 op_sel_hi:[1,0]
	v_pk_fma_f32 v[28:29], v[52:53], s[22:23], v[4:5] op_sel_hi:[1,0,1]
	v_pk_mul_f32 v[24:25], v[26:27], v[24:25]
	v_pk_add_f32 v[26:27], v[32:33], 1.0 op_sel_hi:[1,0]
	v_med3_f32 v28, v28, s87, v189
	v_rcp_f32_e32 v26, v26
	v_rcp_f32_e32 v27, v27
	v_med3_f32 v29, v29, s87, v189
	v_pk_fma_f32 v[16:17], v[48:49], s[22:23], v[16:17] op_sel_hi:[1,0,1]
	v_pk_fma_f32 v[10:11], v[42:43], s[22:23], v[10:11] op_sel_hi:[1,0,1]
	v_pk_mul_f32 v[26:27], v[30:31], v[26:27]
	v_mov_b32_e32 v30, v163
	v_mov_b32_e32 v31, v163
	v_cvt_pk_fp8_f32 v30, v20, v21
	v_cvt_pk_fp8_f32 v31, v24, v25
	v_pk_add_f32 v[20:21], v[28:29], 1.0 op_sel_hi:[1,0]
	v_min_f32_e32 v16, 0x40e00000, v16
	v_pk_mul_f32 v[20:21], v[20:21], v[26:27]
	v_cvt_pk_fp8_f32 v30, v22, v23 op_sel:[0,0,1]
	v_cvt_pk_fp8_f32 v31, v20, v21 op_sel:[0,0,1]
	v_add_co_u32_e32 v20, vcc, s6, v18
	v_min_f32_e32 v17, 0x40e00000, v17
	s_nop 0
	v_addc_co_u32_e32 v21, vcc, 0, v19, vcc
	global_store_dwordx2 v[20:21], v[30:31], off nt
	v_pk_mul_f32 v[20:21], v[14:15], s[24:25] op_sel_hi:[1,0]
	v_pk_mul_f32 v[22:23], v[16:17], s[24:25] op_sel_hi:[1,0]
	v_exp_f32_e32 v20, v20
	v_exp_f32_e32 v21, v21
	v_exp_f32_e32 v22, v22
	v_exp_f32_e32 v23, v23
	v_med3_f32 v10, v10, s87, v189
	v_pk_add_f32 v[20:21], v[20:21], 1.0 op_sel_hi:[1,0]
	v_med3_f32 v11, v11, s87, v189
	v_rcp_f32_e32 v20, v20
	v_rcp_f32_e32 v21, v21
	v_pk_add_f32 v[10:11], v[10:11], 1.0 op_sel_hi:[1,0]
	v_pk_fma_f32 v[12:13], v[44:45], s[22:23], v[12:13] op_sel_hi:[1,0,1]
	v_pk_fma_f32 v[6:7], v[38:39], s[22:23], v[6:7] op_sel_hi:[1,0,1]
	v_pk_mul_f32 v[14:15], v[14:15], v[20:21]
	v_med3_f32 v12, v12, s87, v189
	v_pk_mul_f32 v[10:11], v[10:11], v[14:15]
	v_pk_add_f32 v[14:15], v[22:23], 1.0 op_sel_hi:[1,0]
	v_med3_f32 v13, v13, s87, v189
	v_rcp_f32_e32 v14, v14
	v_rcp_f32_e32 v15, v15
	v_pk_add_f32 v[12:13], v[12:13], 1.0 op_sel_hi:[1,0]
	v_min_f32_e32 v6, 0x40e00000, v6
	v_min_f32_e32 v7, 0x40e00000, v7
	v_pk_mul_f32 v[14:15], v[16:17], v[14:15]
	v_pk_fma_f32 v[8:9], v[40:41], s[22:23], v[8:9] op_sel_hi:[1,0,1]
	v_pk_mul_f32 v[12:13], v[12:13], v[14:15]
	v_pk_mul_f32 v[14:15], v[6:7], s[24:25] op_sel_hi:[1,0]
	v_min_f32_e32 v8, 0x40e00000, v8
	v_exp_f32_e32 v14, v14
	v_exp_f32_e32 v15, v15
	v_min_f32_e32 v9, 0x40e00000, v9
	v_pk_mul_f32 v[16:17], v[8:9], s[24:25] op_sel_hi:[1,0]
	v_pk_fma_f32 v[2:3], v[34:35], s[22:23], v[2:3] op_sel_hi:[1,0,1]
	v_pk_add_f32 v[14:15], v[14:15], 1.0 op_sel_hi:[1,0]
	v_exp_f32_e32 v16, v16
	v_rcp_f32_e32 v14, v14
	v_rcp_f32_e32 v15, v15
	v_exp_f32_e32 v17, v17
	v_med3_f32 v2, v2, s87, v189
	v_med3_f32 v3, v3, s87, v189
	v_pk_mul_f32 v[6:7], v[6:7], v[14:15]
	v_pk_add_f32 v[2:3], v[2:3], 1.0 op_sel_hi:[1,0]
	v_pk_fma_f32 v[4:5], v[36:37], s[22:23], v[4:5] op_sel_hi:[1,0,1]
	v_pk_mul_f32 v[2:3], v[2:3], v[6:7]
	v_pk_add_f32 v[6:7], v[16:17], 1.0 op_sel_hi:[1,0]
	v_med3_f32 v4, v4, s87, v189
	v_rcp_f32_e32 v6, v6
	v_rcp_f32_e32 v7, v7
	v_med3_f32 v5, v5, s87, v189
	v_pk_mul_f32 v[6:7], v[8:9], v[6:7]
	v_mov_b32_e32 v8, v163
	v_mov_b32_e32 v9, v163
	v_cvt_pk_fp8_f32 v8, v10, v11
	v_cvt_pk_fp8_f32 v9, v2, v3
	v_pk_add_f32 v[2:3], v[4:5], 1.0 op_sel_hi:[1,0]
	v_cvt_pk_fp8_f32 v8, v12, v13 op_sel:[0,0,1]
	v_pk_mul_f32 v[2:3], v[2:3], v[6:7]
	s_nop 0
	v_cvt_pk_fp8_f32 v9, v2, v3 op_sel:[0,0,1]
	v_add_co_u32_e32 v2, vcc, 0x58000, v18
	s_nop 1
	v_addc_co_u32_e32 v3, vcc, 0, v19, vcc
	s_andn2_b64 vcc, exec, s[4:5]
	s_mov_b64 s[4:5], -1
	global_store_dwordx2 v[2:3], v[8:9], off nt
	s_cbranch_vccnz .LBB0_1348
	s_andn2_b64 vcc, exec, s[12:13]
	s_cbranch_vccnz .LBB0_1347
	s_barrier
	s_branch .LBB0_1347
